# baseline (speedup 1.0000x reference)
_Z8gemm16_kILi256ELi192ELi0ELi2EEvPKDF16_S1_PvPKfi:
	s_load_dwordx4 s[4:7], s[0:1], 0x0
	v_readfirstlane_b32 s3, v0
	s_cmpk_lt_i32 s3, 0x100
	s_cbranch_scc0 .LBB2_2
	s_setprio 1
